# phase+1 conversion quotas 4->5 (idle WGs), 1->2 (gating WGs): more expert-weight conversion hidden next to the compression MLP
# speedup vs baseline: 1.0153x; 1.0153x over previous
; __global__ void __launch_bounds__(NWAVES * 64, 2) trunk_fwd(Args args) {
;     ...
;         if (EN(2) && IN(pb + 1)) {
;             int tz = threadIdx.x; asm volatile("" : "+v"(tz)); const int lane = tz & 63; const int wave = __builtin_amdgcn_readfirstlane(tz >> 6); const int tid = tz; const int gw = bx * NWAVES + wave; (void)lane; (void)tid; (void)gw;
;             if (bx < 16) {
;                 pg8::Gemm g{FLAT, CW1_T + (size_t)layer * 2 * 256 * 2048, 4096, 256, 2048, (size_t)256 * 2048 * 2}; pg8::CmpOrder S{bx};
;                 pg8::EpiCmp E{HID, CB1 + layer * 512};
;                 pg8::gemm_phase(lds, g, S, E, tz);
;                 __builtin_amdgcn_fence(__ATOMIC_RELEASE, "workgroup"); __syncthreads(); __builtin_amdgcn_fence(__ATOMIC_ACQUIRE, "workgroup");
;                 const int wt = bx * NWAVES + wave;
;                 if (wt < 128) { const int kv = wt >> 6, rb = wt & 63, r32 = lane & 31, hh = lane >> 5;
;                     const bf16* A = HID + (size_t)(kv * 2048 + 32 * rb + r32) * 256; const bf16* W2 = CW2_T + (size_t)(layer * 2 + kv) * 64 * 256;
;                     f32x16 acc[2];
;     #pragma unroll
;                     for (int r = 0; r < 16; ++r) { acc[0][r] = 0.f; acc[1][r] = 0.f; }
;     #pragma unroll 8
;                     for (int ks = 0; ks < 16; ++ks) { const bf16x8 a = *(const bf16x8*)(A + 16 * ks + 8 * hh);
;     #pragma unroll
;                         for (int nb = 0; nb < 2; ++nb) { const bf16x8 bb = *(const bf16x8*)(W2 + (size_t)(32 * nb + r32) * 256 + 16 * ks + 8 * hh); acc[nb] = MFMA32(a, bb, acc[nb]); } }
;     #pragma unroll
;                     for (int nb = 0; nb < 2; ++nb)
;     #pragma unroll
;                         for (int r = 0; r < 16; ++r) { const int rho = 32 * rb + crow(r, hh), b = rho >> 9, c = (rho >> 2) & 127, gg = rho & 3;
;                             KCT[(size_t)kv * 16 * 128 * 64 + (size_t)((b * 4 + gg) * 128 + c) * 64 + 32 * nb + r32] = (bf16)f2bf(acc[nb][r]); } }
;             } else if (bx < 144 || G < 160) {
;                 for (int u = bx - 16; u < 128; u += (G < 160 ? G : 144) - 16)
;                     sgu::unit(lds, Zb, SGW + (size_t)layer * 8 * 128 * 128, args.in[I_LNG] + layer * 1024, args.in[I_LNB] + layer * 1024, args.in[I_SGB] + layer * 1024, OB, u >> 5, (u >> 1) & 15, (u & 1) * 4, 4, tz);
;                 __syncthreads();
.LBB0_253:
	v_readlane_b32 s0, v250, 8
	v_readlane_b32 s1, v250, 9
	s_xor_b64 s[0:1], s[0:1], -1
	v_readlane_b32 s6, v250, 2
	v_writelane_b32 v255, s0, 19
	v_readlane_b32 s7, v250, 3
	s_cmp_gt_i32 s6, s20
	v_writelane_b32 v255, s1, 20
	s_cselect_b64 s[0:1], -1, 0
	s_cmp_ge_i32 s20, s7
	s_cselect_b64 s[4:5], -1, 0
	s_or_b64 s[0:1], s[0:1], s[4:5]
	s_and_b64 vcc, exec, s[0:1]
	s_cbranch_vccnz .LBB0_391
	v_readlane_b32 s4, v251, 38
	v_mov_b32_e32 v1, v0
	v_readlane_b32 s5, v251, 39
	s_mov_b64 s[0:1], -1
	v_readfirstlane_b32 s18, v1
	s_and_b64 vcc, exec, s[4:5]
	s_cbranch_vccz .LBB0_330
	v_readlane_b32 s4, v251, 40
	v_readlane_b32 s5, v251, 41
	s_and_b64 vcc, exec, s[4:5]
	s_cbranch_vccz .LBB0_285
	v_mov_b32_e32 v2, v0
	v_mov_b32_e32 v127, 5
	v_readfirstlane_b32 s12, v2
	v_cmp_eq_u32_e64 s[0:1], 0, v2
	v_mov_b32_e32 v129, -1
	s_and_saveexec_b64 s[4:5], s[0:1]
	s_cbranch_execz .LBB0_264
	s_mov_b64 s[8:9], exec
	v_mbcnt_lo_u32_b32 v3, s8, 0
	v_mbcnt_hi_u32_b32 v3, s9, v3
	v_cmp_eq_u32_e32 vcc, 0, v3
	s_and_saveexec_b64 s[6:7], vcc
	s_cbranch_execz .LBB0_259
	s_bcnt1_i32_b64 s8, s[8:9]
	v_mov_b32_e32 v4, s8
	v_readlane_b32 s8, v250, 18
	v_readlane_b32 s9, v250, 19
	s_nop 4
	global_atomic_add v4, v187, v4, s[8:9] sc0

;     int tid = threadIdx.x; asm volatile("" : "+v"(tid)); const int lane = tid & 63, wave = __builtin_amdgcn_readfirstlane(tid >> 6);
;     unsigned nxt = CQ_END; int left = quota;
.LBB0_263:
	s_or_b64 exec, exec, s[6:7]
	v_mov_b32_e32 v127, 4

;     int tid = threadIdx.x; asm volatile("" : "+v"(tid)); const int lane = tid & 63, wave = __builtin_amdgcn_readfirstlane(tid >> 6);
;     unsigned nxt = CQ_END; int left = quota;
; __global__ void __launch_bounds__(NWAVES * 64, 2) trunk_fwd(Args args) {
;     ...
;                 __syncthreads();
;                 conv_run(args.in[I_M1], args.in[I_M3], args.in[I_M2], MUP_T, MDN_T, ctl, MISC + 16, true, nullptr, 0u, 1);
.LBB0_301:
	v_mov_b32_e32 v2, v0
	s_waitcnt vmcnt(0)
	s_barrier
	v_mov_b32_e32 v127, 2
	v_readfirstlane_b32 s12, v2
	v_cmp_eq_u32_e64 s[0:1], 0, v2
	v_mov_b32_e32 v129, -1
	s_and_saveexec_b64 s[4:5], s[0:1]
	v_readlane_b32 s23, v255, 15
	s_cbranch_execz .LBB0_309
	s_mov_b64 s[8:9], exec
	v_mbcnt_lo_u32_b32 v3, s8, 0
	v_mbcnt_hi_u32_b32 v3, s9, v3
	v_cmp_eq_u32_e32 vcc, 0, v3
	s_and_saveexec_b64 s[6:7], vcc
	s_cbranch_execz .LBB0_304
	s_bcnt1_i32_b64 s8, s[8:9]
	v_mov_b32_e32 v4, s8
	v_readlane_b32 s8, v250, 18
	v_readlane_b32 s9, v250, 19
	s_nop 4
	global_atomic_add v4, v187, v4, s[8:9] sc0

;     int tid = threadIdx.x; asm volatile("" : "+v"(tid)); const int lane = tid & 63, wave = __builtin_amdgcn_readfirstlane(tid >> 6);
;     unsigned nxt = CQ_END; int left = quota;
.LBB0_308:
	s_or_b64 exec, exec, s[6:7]
	v_mov_b32_e32 v127, 1
